# attention-hosted conversion as a quarter unit (4 row loads) per wave per iteration: equal extra work for every wave in every iteration
# speedup vs baseline: 1.0306x; 1.0172x over previous
; #define LAS __attribute__((address_space(3)))
; __device__ __forceinline__ void convert_experts(Frame& F, int lo, int hi) {
;     const int gw = F.vcu * 8 + F.wave, NGW = F.G * 8;
;     LAS unsigned char* scr = F.lds + F.wave * 16384;
;     unsigned char* W1t = WSP(F, WS_W1T, unsigned char); unsigned char* W2t = WSP(F, WS_W2T, unsigned char);
;     const float* weg = F.a->in[I_WEG]; const float* weu = F.a->in[I_WEU]; const float* wed = F.a->in[I_WED];
;     const float* wsg = F.a->in[I_WSG]; const float* wsu = F.a->in[I_WSU]; const float* wsd = F.a->in[I_WSD];
;     ...
;     constexpr int NPAIRS = CONV_ITEMS / 2;
;     (void)lo; (void)hi;
;     ...
;     if (gw < NPAIRS) {
;         const int ns = 2 * ((NPAIRS - gw + NGW - 1) / NGW);
;         int sq = 0, r = CONV_RIDX(0);
;         TItem tc, tn; CONV_DESC(r, tc); tn = tc;
;         int p = 0; bool first = true;
.Lcva_vcu:
	s_lshr_b32 s99, s99, 6
	s_lshl_b32 s101, s101, 3
	s_add_u32 s89, s101, s99
	s_movk_i32 s90, 12
	s_mov_b32 s32, 0
	s_mov_b32 s95, 0
	s_mov_b32 s100, 0
	s_waitcnt vmcnt(0)
	s_branch .LBB0_304

; #define LAS __attribute__((address_space(3)))
; __device__ __forceinline__ void lds_barrier() { asm volatile("s_waitcnt lgkmcnt(0)\n\ts_barrier" ::: "memory"); }
; __device__ __forceinline__ void phase_attn(Frame& F) {
;     ...
;     for (; jl < PER_X; jl += G8) {
;         lds_barrier();
;         LAS unsigned char* kb = F.lds + buf * ABUF;
.LBB0_304:
	s_mul_i32 s37, s79, 0x12000
	s_add_i32 s85, s37, 0
	s_cmp_eq_u32 s100, 0
	s_cbranch_scc1 .Lcq_w3
	s_waitcnt vmcnt(7)
	s_mov_b32 s100, 0
	s_branch .Lcq_wd

; #define LAS __attribute__((address_space(3)))
; __device__ __forceinline__ void lds_barrier() { asm volatile("s_waitcnt lgkmcnt(0)\n\ts_barrier" ::: "memory"); }
; __device__ __forceinline__ void convert_experts(Frame& F, int lo, int hi) {
;     ...
;             const bool more = sq + 1 < ns; const int rn = more ? CONV_RIDX(sq + 1) : r;
;             if (more) { CONV_DESC(rn, tn); titem_issue(tn, F.lane, scr + (p ^ 1) * 8192); }
; __device__ __forceinline__ void phase_attn(Frame& F) {
;     ...
;         lds_barrier();
;         LAS unsigned char* kb = F.lds + buf * ABUF;
;         const bf16x8 q0 = qn0, q1 = qn1;
;         {
;             LAS unsigned char* ob = F.lds + (buf ^ 1) * ABUF;
; #pragma unroll
;             for (int jj = 0; jj < 4; ++jj) { const int ch = tid + 512 * jj, row = ch >> 3, c16 = ch & 7;
;                 *(LAS u32x4*)(ob + row * ATT_ROWB + c16 * 16) = kr[jj]; *(LAS u32x4*)(ob + ATT_VOFF + row * ATT_ROWB + c16 * 16) = vr[jj]; }
;         }
;         const AttnUnit nu = un;
;         un = attn_decode(x8 * PER_X + (jl + 2 * G8 < jlast ? jl + 2 * G8 : jlast)); attn_issue(qkv, un, tid, kr, vr);
;         { const char* qb = (const char*)qkv + (((size_t)nu.b * SEQ + nu.r) * NPROJ + nu.h * 64) * 2; const unsigned qo = __umul24((unsigned)(128 * nu.n + ql), (unsigned)nu.d * (NPROJ * 2)) + 16u * fq;
;           qn0 = *(const bf16x8*)(qb + qo); qn1 = *(const bf16x8*)(qb + qo + 64); }
;         const unsigned qrow = __umul24((unsigned)(128 * cu.n + ql), (unsigned)cu.d);
;         const float c1 = 0.125f * LOG2E;
;         const float nc2 = -__builtin_amdgcn_exp2f(-(float)(cu.h + 1)) * (float)cu.d * LOG2E;
;         const bool first = cu.n == 0;
;         f32x4 St[9];
;         const f32x4 eb = (f32x4){ef[0], ef[1], ef[2], ef[3]} * nc2;
;         float mx = -INFINITY;
;         bf16x8 kf[9][2];
; #pragma unroll
;         for (int T = 0; T < 9; ++T) { LAS unsigned char* ka = kb + (16 * (w + T) + fr) * ATT_ROWB + fq * 16; kf[T][0] = *(LAS bf16x8*)ka; kf[T][1] = *(LAS bf16x8*)(ka + 64); }
.Lcq_wd:
	v_mov_b64_e32 v[48:49], v[4:5]
	v_mov_b64_e32 v[46:47], v[2:3]
	v_mov_b64_e32 v[44:45], v[8:9]
	v_mov_b64_e32 v[42:43], v[6:7]
	s_lshl_b32 s65, 1, s35
	s_waitcnt lgkmcnt(0)
	s_barrier
	s_add_i32 s37, s30, 1
	v_cvt_f32_u32_e32 v54, s37
	v_cvt_f32_u32_e32 v55, s65
	v_add_u32_e32 v110, s85, v82
	v_add_u32_e32 v58, v110, v90
	v_exp_f32_e64 v54, -v54
	v_add_u32_e32 v66, v110, v91
	v_add_u32_e32 v74, v110, v92
	v_add_u32_e32 v111, v110, v93
	v_mul_f32_e32 v79, v55, v54
	ds_read_b128 v[54:57], v58
	ds_read_b128 v[58:61], v58 offset:64
	ds_read_b128 v[62:65], v66
	ds_read_b128 v[66:69], v66 offset:64
	ds_read_b128 v[70:73], v74
	ds_read_b128 v[74:77], v74 offset:64
	ds_read_b128 v[112:115], v111
	ds_read_b128 v[116:119], v111 offset:64
	v_add_u32_e32 v111, v110, v94
	ds_read_b128 v[120:123], v111
	ds_read_b128 v[124:127], v111 offset:64
	v_add_u32_e32 v111, v110, v95
	ds_read_b128 v[128:131], v111
	ds_read_b128 v[132:135], v111 offset:64
	v_add_u32_e32 v111, v110, v96
	ds_read_b128 v[136:139], v111
	ds_read_b128 v[140:143], v111 offset:64
	v_add_u32_e32 v111, v110, v97
	v_add_u32_e32 v110, v110, v98
	ds_read_b128 v[144:147], v111
	ds_read_b128 v[148:151], v111 offset:64
	ds_read_b128 v[152:155], v110
	ds_read_b128 v[156:159], v110 offset:64
	s_sub_u32 s32, s32, 1
	s_cmp_lt_i32 s32, 0
	s_cbranch_scc0 .Lcq_cont_l
	s_mov_b32 s32, 3
	s_mov_b32 s95, 0
	s_cmp_eq_u32 s90, 0
	s_cbranch_scc1 .Lcq_none_l
	s_sub_u32 s90, s90, 1
	s_lshr_b32 s98, s89, 6
	s_and_b32 s99, s89, 63
	s_mul_hi_u32 s100, s98, 0xaaaaaaab
	s_lshr_b32 s100, s100, 1
	s_mul_i32 s101, s100, 3
	s_sub_u32 s101, s98, s101
	s_cmp_lt_u32 s100, 256
	s_cselect_b32 s98, 0, 3
	s_cselect_b32 s95, s100, 0
	s_add_u32 s98, s98, s101
	s_lshl_b32 s98, s98, 1
	v_readlane_b32 s96, v253, s98
	s_add_u32 s98, s98, 1
	v_readlane_b32 s97, v253, s98
	s_lshl_b32 s95, s95, 20
	s_nop 3
	s_add_u32 s96, s96, s95
	s_addc_u32 s97, s97, 0
	s_cmp_eq_u32 s101, 2
	s_cbranch_scc1 .Lcq_down_l
	s_lshr_b32 s95, s99, 3
	s_and_b32 s99, s99, 7
	s_lshl_b32 s98, s95, 17
	s_add_u32 s96, s96, s98
	s_addc_u32 s97, s97, 0
	s_lshl_b32 s98, s99, 7
	s_add_u32 s96, s96, s98
	s_addc_u32 s97, s97, 0
	s_lshl_b32 s100, s100, 19
	s_lshr_b32 s98, s99, 2
	s_lshl_b32 s98, s98, 18
	s_add_u32 s100, s100, s98
	s_and_b32 s98, s99, 3
	s_lshl_b32 s98, s98, 15
	s_add_u32 s100, s100, s98
	s_lshl_b32 s98, s101, 17
	s_add_u32 s100, s100, s98
	s_lshl_b32 s98, s95, 7
	s_add_u32 s100, s100, s98
	v_readlane_b32 s92, v253, 12
	v_readlane_b32 s93, v253, 13
	s_mov_b32 s94, 0xc3317218
	s_cmp_eq_u32 s101, 0
	s_cselect_b32 s94, 0xc2b8aa3b, s94
	s_nop 3
	s_add_u32 s92, s92, s100
	s_addc_u32 s93, s93, 0
	s_movk_i32 s95, 0x400
	s_movk_i32 s98, 0x400
	s_branch .Lcq_go_l

; #define LAS __attribute__((address_space(3)))
; __device__ __forceinline__ void titem_issue(const TItem& t, int lane, LAS unsigned char* buf) {
;     const int nblk = t.N / 32, kb = t.item / nblk, nb = t.item % nblk, k0 = 64 * kb, n0 = 32 * nb;
; #pragma unroll
;     for (int j = 0; j < 8; ++j) { const float* g = t.W + (size_t)(k0 + 8 * j + (lane >> 3)) * t.N + n0 + 4 * ((lane & 7) ^ j);
;         __builtin_amdgcn_global_load_lds((const unsigned*)g, (LAS unsigned*)(buf + j * 1024), 16, 0, 2); }
; }
; __device__ __forceinline__ void phase_attn(Frame& F) {
;     ...
; #pragma unroll
;         for (int T = 0; T < 9; ++T) { LAS unsigned char* ka = kb + (16 * (w + T) + fr) * ATT_ROWB + fq * 16; kf[T][0] = *(LAS bf16x8*)ka; kf[T][1] = *(LAS bf16x8*)(ka + 64); }
;         __builtin_amdgcn_sched_barrier(0);
; #pragma unroll
;         for (int T = 0; T < 9; ++T) {
;             f32x4 sa = (f32x4){0.f, 0.f, 0.f, 0.f};
;             sa = __builtin_amdgcn_mfma_f32_16x16x32_bf16(kf[T][0], q0, sa, 0, 0, 0);
;             sa = __builtin_amdgcn_mfma_f32_16x16x32_bf16(kf[T][1], q1, sa, 0, 0, 0);
;             const float kT = (!first || w + T >= 8) ? nc2 * (float)(128 - 16 * T) : -INFINITY;
;             sa = sa * c1 + (eb + kT);
; #pragma unroll
;             for (int rg = 0; rg < 4; ++rg) {
;                 if (T == 0) sa[rg] = ef[rg] <= 0.f ? sa[rg] : -INFINITY;
;                 if (T == 8) sa[rg] = ef[rg] >= 0.f ? sa[rg] : -INFINITY;
;             }
;             St[T] = sa;
;             mx = fmaxf(mx, fmaxf(fmaxf(sa[0], sa[1]), fmaxf(sa[2], sa[3])));
;         }
.Lcq_go_l:
	s_mov_b32 s100, 0
	s_lshl_b32 s99, s69, 6
	s_add_u32 s89, s89, s99
.Lcq_cont_l:
	s_cmp_eq_u32 s95, 0
	s_cbranch_scc1 .Lcq_none_l
	s_lshl_b32 s99, s98, 4
	v_mad_u32_u24 v250, v248, s99, v249
	global_load_dwordx4 v[168:171], v250, s[96:97] nt
	s_add_u32 s96, s96, s98
	s_addc_u32 s97, s97, 0
	global_load_dwordx4 v[172:175], v250, s[96:97] nt
	s_add_u32 s96, s96, s98
	s_addc_u32 s97, s97, 0
	global_load_dwordx4 v[176:179], v250, s[96:97] nt
	s_add_u32 s96, s96, s98
	s_addc_u32 s97, s97, 0
	global_load_dwordx4 v[180:183], v250, s[96:97] nt
	s_add_u32 s96, s96, s98
	s_addc_u32 s97, s97, 0
.Lcq_none_l:
	s_cmp_lg_u32 s64, 0
	v_lshl_add_u32 v78, s64, 7, v86
	s_cselect_b64 s[64:65], -1, 0
	v_mul_f32_e32 v160, 0xbfb8aa3b, v79
	v_and_b32_e32 v110, 0xffffff, v78
	s_waitcnt lgkmcnt(14)
	v_mfma_f32_16x16x32_bf16 v[54:57], v[54:57], v[46:49], 0
	v_mul_f32_e32 v78, 0x43000000, v160
	s_or_b64 vcc, s[64:65], s[38:39]
	v_cndmask_b32_e32 v78, v109, v78, vcc
	v_mfma_f32_16x16x32_bf16 v[54:57], v[58:61], v[42:45], v[54:57]
	v_fma_f32 v162, v50, v160, v78
	v_fma_f32 v163, v51, v160, v78
	v_pk_fma_f32 v[78:79], v[52:53], v[160:161], v[78:79] op_sel_hi:[1,0,0]
	s_or_b64 vcc, s[64:65], s[40:41]
	s_nop 3
	v_pk_fma_f32 v[56:57], v[56:57], s[56:57], v[78:79] op_sel_hi:[1,0,1]
	v_pk_fma_f32 v[54:55], v[54:55], s[56:57], v[162:163] op_sel_hi:[1,0,1]
	v_cndmask_b32_e64 v164, v109, v56, s[10:11]
	v_cndmask_b32_e64 v162, v109, v54, s[6:7]
	v_cndmask_b32_e64 v163, v109, v55, s[8:9]
	v_cndmask_b32_e64 v165, v109, v57, s[12:13]
	v_mfma_f32_16x16x32_bf16 v[54:57], v[62:65], v[46:49], 0
	v_max_f32_e32 v58, v162, v163
	v_max_f32_e32 v59, v164, v165
	v_max3_f32 v62, v58, v59, s78
	v_mfma_f32_16x16x32_bf16 v[54:57], v[66:69], v[42:45], v[54:57]
	v_mul_f32_e32 v58, 0x42e00000, v160
	v_cndmask_b32_e32 v58, v109, v58, vcc
	v_pk_fma_f32 v[60:61], v[50:51], v[160:161], v[58:59] op_sel_hi:[1,0,0]
	v_pk_fma_f32 v[58:59], v[52:53], v[160:161], v[58:59] op_sel_hi:[1,0,0]
	s_or_b64 vcc, s[64:65], s[42:43]
	s_nop 2
	v_pk_fma_f32 v[166:167], v[56:57], s[56:57], v[58:59] op_sel_hi:[1,0,1]
	s_waitcnt lgkmcnt(13)
	v_mfma_f32_16x16x32_bf16 v[56:59], v[70:73], v[46:49], 0
	v_fma_f32 v78, v54, s56, v60
	v_fma_f32 v79, v55, s56, v61
	v_max_f32_e32 v54, v166, v167
	v_max3_f32 v63, v78, v79, v54
	s_waitcnt lgkmcnt(12)
	v_mfma_f32_16x16x32_bf16 v[54:57], v[74:77], v[42:45], v[56:59]
	s_nop 2
	v_mul_f32_e32 v58, 0x42c00000, v160
	v_cndmask_b32_e32 v58, v109, v58, vcc
	v_pk_fma_f32 v[60:61], v[50:51], v[160:161], v[58:59] op_sel_hi:[1,0,0]
	v_pk_fma_f32 v[58:59], v[52:53], v[160:161], v[58:59] op_sel_hi:[1,0,0]
	s_nop 0
	v_pk_fma_f32 v[76:77], v[54:55], s[56:57], v[60:61] op_sel_hi:[1,0,1]
	v_pk_fma_f32 v[74:75], v[56:57], s[56:57], v[58:59] op_sel_hi:[1,0,1]
	s_waitcnt lgkmcnt(11)
	v_mfma_f32_16x16x32_bf16 v[54:57], v[112:115], v[46:49], 0
	v_max_f32_e32 v58, v74, v75
	v_max3_f32 v58, v76, v77, v58
	v_max3_f32 v62, v62, v63, v58
	s_waitcnt lgkmcnt(10)
	v_mfma_f32_16x16x32_bf16 v[54:57], v[116:119], v[42:45], v[54:57]
	v_mul_f32_e32 v58, 0x42a00000, v160
	s_or_b64 vcc, s[64:65], s[44:45]
	v_cndmask_b32_e32 v58, v109, v58, vcc
	v_pk_fma_f32 v[60:61], v[50:51], v[160:161], v[58:59] op_sel_hi:[1,0,0]
	v_pk_fma_f32 v[58:59], v[52:53], v[160:161], v[58:59] op_sel_hi:[1,0,0]
	s_nop 2
	v_pk_fma_f32 v[72:73], v[54:55], s[56:57], v[60:61] op_sel_hi:[1,0,1]
	v_pk_fma_f32 v[70:71], v[56:57], s[56:57], v[58:59] op_sel_hi:[1,0,1]
	s_waitcnt lgkmcnt(9)
	v_mfma_f32_16x16x32_bf16 v[56:59], v[120:123], v[46:49], 0
	v_max_f32_e32 v54, v70, v71
	v_max3_f32 v63, v72, v73, v54
	s_or_b64 vcc, s[64:65], s[46:47]
	s_waitcnt lgkmcnt(8)
	v_mfma_f32_16x16x32_bf16 v[54:57], v[124:127], v[42:45], v[56:59]
	s_nop 2
	v_mul_f32_e32 v58, 0x42800000, v160
	v_cndmask_b32_e32 v58, v109, v58, vcc
	v_pk_fma_f32 v[60:61], v[50:51], v[160:161], v[58:59] op_sel_hi:[1,0,0]
	v_pk_fma_f32 v[58:59], v[52:53], v[160:161], v[58:59] op_sel_hi:[1,0,0]
	s_nop 0
	v_pk_fma_f32 v[68:69], v[54:55], s[56:57], v[60:61] op_sel_hi:[1,0,1]
	v_pk_fma_f32 v[66:67], v[56:57], s[56:57], v[58:59] op_sel_hi:[1,0,1]
	s_waitcnt lgkmcnt(7)
	v_mfma_f32_16x16x32_bf16 v[54:57], v[128:131], v[46:49], 0
	v_max_f32_e32 v58, v66, v67
	v_max3_f32 v58, v68, v69, v58
	v_max3_f32 v111, v62, v63, v58
	s_waitcnt lgkmcnt(6)
	v_mfma_f32_16x16x32_bf16 v[54:57], v[132:135], v[42:45], v[54:57]
	v_mul_f32_e32 v58, 0x42400000, v160
	s_or_b64 vcc, s[64:65], s[48:49]
	v_cndmask_b32_e32 v58, v109, v58, vcc
	v_pk_fma_f32 v[60:61], v[50:51], v[160:161], v[58:59] op_sel_hi:[1,0,0]
	v_pk_fma_f32 v[58:59], v[52:53], v[160:161], v[58:59] op_sel_hi:[1,0,0]
	s_nop 2
	v_pk_fma_f32 v[64:65], v[54:55], s[56:57], v[60:61] op_sel_hi:[1,0,1]
	v_pk_fma_f32 v[62:63], v[56:57], s[56:57], v[58:59] op_sel_hi:[1,0,1]
	s_waitcnt lgkmcnt(5)
	v_mfma_f32_16x16x32_bf16 v[56:59], v[136:139], v[46:49], 0
	v_max_f32_e32 v54, v62, v63
	v_max3_f32 v112, v64, v65, v54
	s_or_b64 vcc, s[64:65], s[50:51]
	s_waitcnt lgkmcnt(4)
	v_mfma_f32_16x16x32_bf16 v[54:57], v[140:143], v[42:45], v[56:59]
	s_nop 2
	v_mul_f32_e32 v58, 0x42000000, v160
	v_cndmask_b32_e32 v58, v109, v58, vcc
	v_pk_fma_f32 v[60:61], v[50:51], v[160:161], v[58:59] op_sel_hi:[1,0,0]
	v_pk_fma_f32 v[58:59], v[52:53], v[160:161], v[58:59] op_sel_hi:[1,0,0]
	s_nop 0
	v_pk_fma_f32 v[60:61], v[54:55], s[56:57], v[60:61] op_sel_hi:[1,0,1]
	v_pk_fma_f32 v[58:59], v[56:57], s[56:57], v[58:59] op_sel_hi:[1,0,1]
	s_waitcnt lgkmcnt(3)
	v_mfma_f32_16x16x32_bf16 v[54:57], v[144:147], v[46:49], 0
	v_max_f32_e32 v113, v58, v59
	v_max3_f32 v113, v60, v61, v113
	v_max3_f32 v111, v111, v112, v113
	s_waitcnt lgkmcnt(1)
; __device__ __forceinline__ void phase_attn(Frame& F) {
;     ...
;             LAS unsigned char* ob = F.lds + (buf ^ 1) * ABUF;
; #pragma unroll
;             for (int jj = 0; jj < 4; ++jj) { const int ch = tid + 512 * jj, row = ch >> 3, c16 = ch & 7;
;                 *(LAS u32x4*)(ob + row * ATT_ROWB + c16 * 16) = kr[jj]; *(LAS u32x4*)(ob + ATT_VOFF + row * ATT_ROWB + c16 * 16) = vr[jj]; }
;         }
;         const AttnUnit nu = un;
;         un = attn_decode(x8 * PER_X + (jl + 2 * G8 < jlast ? jl + 2 * G8 : jlast)); attn_issue(qkv, un, tid, kr, vr);
;         { const char* qb = (const char*)qkv + (((size_t)nu.b * SEQ + nu.r) * NPROJ + nu.h * 64) * 2; const unsigned qo = __umul24((unsigned)(128 * nu.n + ql), (unsigned)nu.d * (NPROJ * 2)) + 16u * fq;
;           qn0 = *(const bf16x8*)(qb + qo); qn1 = *(const bf16x8*)(qb + qo + 64); }
;         const unsigned qrow = __umul24((unsigned)(128 * cu.n + ql), (unsigned)cu.d);
;         const float c1 = 0.125f * LOG2E;
;         const float nc2 = -__builtin_amdgcn_exp2f(-(float)(cu.h + 1)) * (float)cu.d * LOG2E;
;         const bool first = cu.n == 0;
;         f32x4 St[9];
;         const f32x4 eb = (f32x4){ef[0], ef[1], ef[2], ef[3]} * nc2;
;         float mx = -INFINITY;
;         bf16x8 kf[9][2];
; #pragma unroll
;         for (int T = 0; T < 9; ++T) { LAS unsigned char* ka = kb + (16 * (w + T) + fr) * ATT_ROWB + fq * 16; kf[T][0] = *(LAS bf16x8*)ka; kf[T][1] = *(LAS bf16x8*)(ka + 64); }
;         __builtin_amdgcn_sched_barrier(0);
; #pragma unroll
;         for (int T = 0; T < 9; ++T) {
;             f32x4 sa = (f32x4){0.f, 0.f, 0.f, 0.f};
;             sa = __builtin_amdgcn_mfma_f32_16x16x32_bf16(kf[T][0], q0, sa, 0, 0, 0);
;             sa = __builtin_amdgcn_mfma_f32_16x16x32_bf16(kf[T][1], q1, sa, 0, 0, 0);
;             const float kT = (!first || w + T >= 8) ? nc2 * (float)(128 - 16 * T) : -INFINITY;
;             sa = sa * c1 + (eb + kT);
; #pragma unroll
;             for (int rg = 0; rg < 4; ++rg) {
;                 if (T == 0) sa[rg] = ef[rg] <= 0.f ? sa[rg] : -INFINITY;
;                 if (T == 8) sa[rg] = ef[rg] >= 0.f ? sa[rg] : -INFINITY;
;             }
;             St[T] = sa;
;             mx = fmaxf(mx, fmaxf(fmaxf(sa[0], sa[1]), fmaxf(sa[2], sa[3])));
;         }
;         mx = fmaxf(mx, __shfl_xor(mx, 16)); mx = fmaxf(mx, __shfl_xor(mx, 32));
;         f32x4 lv = (f32x4){0.f, 0.f, 0.f, 0.f};
	v_mfma_f32_16x16x32_bf16 v[46:49], v[152:155], v[46:49], 0
	s_or_b64 vcc, s[64:65], s[52:53]
	v_add_u32_e32 v144, s85, v89
	v_add_u32_e32 v130, v144, v99
	v_mfma_f32_16x16x32_bf16 v[112:115], v[148:151], v[42:45], v[54:57]
	v_add_u32_e32 v140, v144, v100
	v_add_u32_e32 v145, v144, v101
	s_nop 0
	v_mul_f32_e32 v54, 0x41800000, v160
	s_waitcnt lgkmcnt(0)
	v_mfma_f32_16x16x32_bf16 v[42:45], v[156:159], v[42:45], v[46:49]
	s_add_i32 s37, s77, s70
	s_xor_b32 s79, s79, 1
	s_min_i32 s37, s37, s71
	s_mul_i32 s58, s79, 0x12000
	s_add_i32 s37, s37, s3
	v_add_u32_e32 v2, s58, v84
	s_mul_hi_i32 s58, s37, 0x2aaaaaab
	s_lshr_b32 s59, s58, 31
	s_ashr_i32 s58, s58, 4
	s_add_i32 s59, s58, s59
	s_mul_i32 s58, s59, 0x60
	s_sub_i32 s37, s37, s58
	s_ashr_i32 s58, s59, 3
	s_and_b32 s80, s59, 7
	v_add_u32_e32 v3, v2, v83
	s_cmp_gt_i32 s37, 31
	ds_write_b128 v3, v[38:41]
	ds_write_b128 v3, v[34:37] offset:36864
	v_add_u32_e32 v3, v2, v85
	s_cselect_b64 s[82:83], -1, 0
	s_cmp_gt_i32 s37, 63
	ds_write_b128 v3, v[30:33]
	ds_write_b128 v3, v[26:29] offset:36864
	v_add_u32_e32 v3, v2, v87
	v_add_u32_e32 v2, v2, v88
	s_cselect_b64 s[86:87], -1, 0
	ds_write_b128 v3, v[22:25]
	ds_write_b128 v3, v[18:21] offset:36864
	ds_write_b128 v2, v[14:17]
	ds_write_b128 v2, v[10:13] offset:36864
	v_cndmask_b32_e64 v2, 0, 1, s[86:87]
	s_cmp_lg_u64 s[82:83], 0
	v_readfirstlane_b32 s59, v2
	s_addc_u32 s81, s59, 0
	s_lshl_b32 s59, s81, 5
	s_lshl_b32 s82, s81, 1
	s_sub_i32 s37, s37, s59
	s_sub_i32 s59, 5, s82
	s_ashr_i32 s83, s37, s59
	s_lshl_b32 s59, -1, s59
	s_andn2_b32 s84, s37, s59
	s_ashr_i32 s59, s58, 31
	s_lshl_b64 s[86:87], s[58:59], 12
	s_ashr_i32 s37, s83, 31
	s_add_u32 s59, s86, s83
	s_addc_u32 s37, s87, s37
	s_mulk_i32 s37, 0xa00
	s_mul_hi_u32 s86, s59, 0xa00
	s_add_i32 s87, s86, s37
	s_mulk_i32 s59, 0xa00
	s_lshl_b32 s37, s80, 6
	s_or_b32 s86, s59, s37
	s_lshl_b64 s[86:87], s[86:87], 1
	s_add_u32 s37, s33, s86
	s_addc_u32 s59, s66, s87
	s_add_u32 s86, s37, 0x400
	s_addc_u32 s87, s59, 0
	s_lshl_b32 s59, s84, 7
	v_add_u32_e32 v2, s59, v81
	s_lshl_b32 s37, 0x1400, s82
	v_max_i32_e32 v3, 0, v2
	v_mul_u32_u24_e32 v3, s37, v3
	v_or_b32_e32 v3, v3, v80
	global_load_dwordx4 v[38:41], v3, s[86:87]
	global_load_dwordx4 v[34:37], v3, s[86:87] offset:1024
	v_max_i32_e32 v3, 0xffffffc0, v2
	v_add_u32_e32 v3, 64, v3
	v_mul_u32_u24_e32 v3, s37, v3
	v_or_b32_e32 v3, v3, v80
	global_load_dwordx4 v[30:33], v3, s[86:87]
	global_load_dwordx4 v[26:29], v3, s[86:87] offset:1024
	v_add_u32_e32 v3, s59, v1
	v_max_i32_e32 v2, 0xffffff40, v2
	v_max_i32_e32 v3, 0, v3
	v_add_u32_e32 v2, 0xc0, v2
	v_mul_u32_u24_e32 v3, s37, v3
	v_mul_u32_u24_e32 v2, s37, v2
	v_or_b32_e32 v3, v3, v80
	v_or_b32_e32 v2, v2, v80
	s_ashr_i32 s37, s36, 31
	global_load_dwordx4 v[22:25], v3, s[86:87]
	global_load_dwordx4 v[18:21], v3, s[86:87] offset:1024
	global_load_dwordx4 v[14:17], v2, s[86:87]
	global_load_dwordx4 v[10:13], v2, s[86:87] offset:1024
	s_lshl_b64 s[86:87], s[36:37], 12
	s_ashr_i32 s37, s73, 31
	s_add_u32 s59, s86, s73
	s_addc_u32 s37, s87, s37
	s_mulk_i32 s37, 0xa00
	s_mul_hi_u32 s86, s59, 0xa00
	s_add_i32 s87, s86, s37
	s_mulk_i32 s59, 0xa00
	s_lshl_b32 s37, s75, 6
	s_or_b32 s86, s59, s37
	s_lshl_b64 s[86:87], s[86:87], 1
	s_add_u32 s86, s33, s86
	s_addc_u32 s87, s66, s87
	s_lshl_b32 s37, 0x1400, s74
	v_lshl_add_u32 v2, s76, 7, v86
	s_and_b32 s37, s37, 0x555400
	v_mul_u32_u24_e32 v2, s37, v2
	v_or_b32_e32 v6, v2, v82
	global_load_dwordx4 v[2:5], v6, s[86:87]
	s_nop 0
	global_load_dwordx4 v[6:9], v6, s[86:87] offset:64
	v_cndmask_b32_e32 v54, v109, v54, vcc
	s_or_b64 vcc, s[64:65], s[54:55]
	v_pk_fma_f32 v[56:57], v[50:51], v[160:161], v[54:55] op_sel_hi:[1,0,0]
	v_mul_f32_e32 v46, 0, v160
	v_cndmask_b32_e32 v46, v109, v46, vcc
	v_pk_fma_f32 v[48:49], v[50:51], v[160:161], v[46:47] op_sel_hi:[1,0,0]
	v_pk_fma_f32 v[46:47], v[52:53], v[160:161], v[46:47] op_sel_hi:[1,0,0]
	v_pk_fma_f32 v[54:55], v[52:53], v[160:161], v[54:55] op_sel_hi:[1,0,0]
	v_pk_fma_f32 v[44:45], v[44:45], s[56:57], v[46:47] op_sel_hi:[1,0,1]
	v_pk_fma_f32 v[42:43], v[42:43], s[56:57], v[48:49] op_sel_hi:[1,0,1]
	v_cndmask_b32_e64 v48, v109, v44, s[18:19]
	v_and_b32_e32 v44, 64, v108
	v_pk_fma_f32 v[54:55], v[114:115], s[56:57], v[54:55] op_sel_hi:[1,0,1]
	v_cndmask_b32_e64 v47, v109, v43, s[16:17]
	v_cndmask_b32_e64 v49, v109, v45, s[20:21]
	v_xor_b32_e32 v43, 16, v108
	v_add_u32_e32 v44, 64, v44
	v_pk_fma_f32 v[56:57], v[112:113], s[56:57], v[56:57] op_sel_hi:[1,0,1]
	v_max_f32_e32 v112, v54, v55
	v_cndmask_b32_e64 v46, v109, v42, s[14:15]
	v_max_f32_e32 v42, v48, v49
	v_cmp_lt_i32_e32 vcc, v43, v44
	v_max3_f32 v112, v56, v57, v112
	v_max3_f32 v42, v46, v47, v42
	v_cndmask_b32_e32 v43, v108, v43, vcc
	v_max3_f32 v42, v111, v112, v42
	v_lshlrev_b32_e32 v142, 2, v43
	ds_bpermute_b32 v43, v142, v42
	s_waitcnt lgkmcnt(0)
	v_max_f32_e32 v43, v43, v43
	v_max_f32_e32 v42, v42, v43
	v_xor_b32_e32 v43, 32, v108
	v_cmp_lt_i32_e32 vcc, v43, v44
	s_nop 1
	v_cndmask_b32_e32 v43, v108, v43, vcc
	v_lshlrev_b32_e32 v143, 2, v43
	ds_bpermute_b32 v43, v143, v42
	s_waitcnt lgkmcnt(0)
	v_max_f32_e32 v43, v43, v43
	v_max_f32_e32 v111, v42, v43
	v_xor_b32_e32 v42, 0x80000000, v111
	v_mov_b32_e32 v43, v42
	v_mov_b32_e32 v44, v42
	v_mov_b32_e32 v45, v42
	ds_read_b64_tr_b16 v[120:121], v130 offset:36864
	v_pk_add_f32 v[118:119], v[166:167], v[44:45]
	v_pk_add_f32 v[112:113], v[164:165], v[44:45]
	v_exp_f32_e32 v126, v118
	v_exp_f32_e32 v127, v119
	ds_read_b64_tr_b16 v[118:119], v130 offset:36872
	v_pk_add_f32 v[114:115], v[162:163], v[42:43]
	v_exp_f32_e32 v112, v112
	v_exp_f32_e32 v114, v114
	v_exp_f32_e32 v113, v113
	v_exp_f32_e32 v115, v115
	ds_read_b64_tr_b16 v[128:129], v130 offset:36928
	ds_read_b64_tr_b16 v[130:131], v130 offset:36936
	v_pk_add_f32 v[134:135], v[76:77], v[42:43]
	v_cvt_pk_bf16_f32 v123, v112, v113
	v_cvt_pk_bf16_f32 v122, v114, v115
	v_pk_add_f32 v[116:117], v[112:113], 0 op_sel_hi:[1,0]
	v_pk_add_f32 v[124:125], v[114:115], 0 op_sel_hi:[1,0]
	s_waitcnt lgkmcnt(3)
; #define LAS __attribute__((address_space(3)))
; __device__ __forceinline__ unsigned cvt_pk_bf16(float lo, float hi) { const f32x2_t v = {lo, hi}; return __builtin_bit_cast(unsigned, __builtin_convertvector(v, bf16x2_t)); }
; __device__ __forceinline__ float fast_exp2(float x) { return __builtin_amdgcn_exp2f(x); }
; __device__ __forceinline__ s16x4 tr_read(LAS unsigned char* p) { return __builtin_bit_cast(s16x4, __builtin_amdgcn_ds_read_tr16_b64_v4i16((LAS s16x4*)p)); }
; __device__ __forceinline__ void phase_attn(Frame& F) {
;     ...
;         for (int T = 0; T < 9; ++T) { const f32x4 d = St[T] + nmx; f32x4 pv; pv.x = fast_exp2(d.x); pv.y = fast_exp2(d.y); pv.z = fast_exp2(d.z); pv.w = fast_exp2(d.w); St[T] = pv; lv = lv + pv; }
;         float l = (lv.x + lv.y) + (lv.z + lv.w);
;         l += __shfl_xor(l, 16); l += __shfl_xor(l, 32);
;         f32x4 O[4];
; #pragma unroll
;         for (int dt = 0; dt < 4; ++dt) O[dt] = (f32x4){0.f, 0.f, 0.f, 0.f};
; #pragma unroll
;         for (int T = 0; T < 9; ++T) {
;             u32x2 pw; pw.x = cvt_pk_bf16(St[T][0], St[T][1]); pw.y = cvt_pk_bf16(St[T][2], St[T][3]);
;             const s16x4 pb = __builtin_bit_cast(s16x4, pw);
;             LAS unsigned char* va = kb + ATT_VOFF + (16 * (w + T) + 4 * fq + (fr >> 2)) * ATT_ROWB + (8 * (fr & 3)) * 2;
; #pragma unroll
;             for (int dt = 0; dt < 4; ++dt) O[dt] = __builtin_amdgcn_mfma_f32_16x16x16bf16_1k(tr_read(va + 64 * (dt >> 1) + 8 * (dt & 1)), pb, O[dt], 0, 0, 0);
;         }
	v_mfma_f32_16x16x16_bf16 v[112:115], v[120:121], v[122:123], 0
	v_add_f32_e64 v120, v74, v44
	v_add_f32_e64 v121, v75, v45
	v_pk_add_f32 v[132:133], v[126:127], v[116:117]
	v_exp_f32_e32 v136, v120
	s_waitcnt lgkmcnt(2)
	v_mfma_f32_16x16x16_bf16 v[116:119], v[118:119], v[122:123], 0
	v_exp_f32_e32 v137, v121
	v_pk_add_f32 v[78:79], v[78:79], v[42:43]
	v_cvt_pk_bf16_f32 v139, v126, v127
	s_waitcnt lgkmcnt(1)
	v_mfma_f32_16x16x16_bf16 v[74:77], v[128:129], v[122:123], 0
	ds_read_b64_tr_b16 v[128:129], v140 offset:36864
	v_exp_f32_e32 v78, v78
	v_exp_f32_e32 v79, v79
	s_waitcnt lgkmcnt(1)
	v_mfma_f32_16x16x16_bf16 v[120:123], v[130:131], v[122:123], 0
	ds_read_b64_tr_b16 v[130:131], v140 offset:36872
	ds_read_b64_tr_b16 v[126:127], v140 offset:36928
	ds_read_b64_tr_b16 v[140:141], v140 offset:36936
	v_cvt_pk_bf16_f32 v138, v78, v79
	v_exp_f32_e32 v134, v134
	v_exp_f32_e32 v135, v135
	s_waitcnt lgkmcnt(3)
	v_mfma_f32_16x16x16_bf16 v[112:115], v[128:129], v[138:139], v[112:115]
	v_add_f32_e64 v128, v70, v44
	v_add_f32_e64 v129, v71, v45
	v_pk_add_f32 v[78:79], v[78:79], v[124:125]
	v_pk_add_f32 v[124:125], v[136:137], v[132:133]
	s_waitcnt lgkmcnt(2)
	v_mfma_f32_16x16x16_bf16 v[116:119], v[130:131], v[138:139], v[116:119]
	v_add_f32_e64 v130, v72, v42
	v_add_f32_e64 v131, v73, v43
	v_pk_add_f32 v[78:79], v[134:135], v[78:79]
	v_exp_f32_e32 v128, v128
	s_waitcnt lgkmcnt(1)
	v_mfma_f32_16x16x16_bf16 v[70:73], v[126:127], v[138:139], v[74:77]
	ds_read_b64_tr_b16 v[126:127], v145 offset:36864
	v_exp_f32_e32 v129, v129
	v_pk_add_f32 v[48:49], v[44:45], v[48:49]
	s_waitcnt lgkmcnt(1)
	v_mfma_f32_16x16x16_bf16 v[74:77], v[140:141], v[138:139], v[120:123]
	v_add_f32_e64 v124, v128, v124
	v_add_f32_e64 v125, v129, v125
	s_nop 0
	ds_read_b64_tr_b16 v[120:121], v145 offset:36872
	v_cvt_pk_bf16_f32 v122, v134, v135
	ds_read_b64_tr_b16 v[132:133], v145 offset:36928
	ds_read_b64_tr_b16 v[134:135], v145 offset:36936
	v_cvt_pk_bf16_f32 v123, v136, v137
	v_add_u32_e32 v136, v144, v102
	s_waitcnt lgkmcnt(3)
	v_mfma_f32_16x16x16_bf16 v[112:115], v[126:127], v[122:123], v[112:115]
	v_exp_f32_e32 v126, v130
	v_exp_f32_e32 v127, v131
	v_pk_add_f32 v[130:131], v[68:69], v[42:43]
	s_waitcnt lgkmcnt(2)
	v_mfma_f32_16x16x16_bf16 v[116:119], v[120:121], v[122:123], v[116:119]
	v_add_f32_e64 v120, v66, v44
	v_add_f32_e64 v121, v67, v45
	v_pk_add_f32 v[78:79], v[126:127], v[78:79]
	v_exp_f32_e32 v130, v130
	s_waitcnt lgkmcnt(1)
	v_mfma_f32_16x16x16_bf16 v[66:69], v[132:133], v[122:123], v[70:73]
	ds_read_b64_tr_b16 v[132:133], v136 offset:36864
	v_exp_f32_e32 v120, v120
	v_exp_f32_e32 v121, v121
	s_waitcnt lgkmcnt(1)
	v_mfma_f32_16x16x16_bf16 v[70:73], v[134:135], v[122:123], v[74:77]
	ds_read_b64_tr_b16 v[122:123], v136 offset:36872
	v_cvt_pk_bf16_f32 v134, v126, v127
	v_cvt_pk_bf16_f32 v135, v128, v129
	ds_read_b64_tr_b16 v[128:129], v136 offset:36928
	ds_read_b64_tr_b16 v[136:137], v136 offset:36936
	s_waitcnt lgkmcnt(3)
	v_mfma_f32_16x16x16_bf16 v[74:77], v[132:133], v[134:135], v[112:115]
	v_add_u32_e32 v132, v144, v103
	ds_read_b64_tr_b16 v[126:127], v132 offset:36872
	v_exp_f32_e32 v131, v131
	s_waitcnt lgkmcnt(3)
	v_mfma_f32_16x16x16_bf16 v[112:115], v[122:123], v[134:135], v[116:119]
	ds_read_b64_tr_b16 v[122:123], v132 offset:36864
	v_pk_add_f32 v[124:125], v[120:121], v[124:125]
	v_pk_add_f32 v[78:79], v[130:131], v[78:79]
	v_pk_add_f32 v[116:117], v[62:63], v[44:45]
	v_pk_add_f32 v[118:119], v[64:65], v[42:43]
	s_waitcnt lgkmcnt(3)
	v_mfma_f32_16x16x16_bf16 v[62:65], v[128:129], v[134:135], v[66:69]
	v_exp_f32_e32 v116, v116
	v_exp_f32_e32 v117, v117
	v_cvt_pk_bf16_f32 v128, v130, v131
	v_cvt_pk_bf16_f32 v129, v120, v121
	ds_read_b64_tr_b16 v[120:121], v132 offset:36928
	ds_read_b64_tr_b16 v[130:131], v132 offset:36936
	v_add_u32_e32 v132, v144, v104
	s_waitcnt lgkmcnt(4)
	v_mfma_f32_16x16x16_bf16 v[66:69], v[136:137], v[134:135], v[70:73]
	v_exp_f32_e32 v118, v118
	v_exp_f32_e32 v119, v119
	s_waitcnt lgkmcnt(2)
	v_mfma_f32_16x16x16_bf16 v[70:73], v[122:123], v[128:129], v[74:77]
	v_add_f32_e64 v122, v116, v124
	v_add_f32_e64 v123, v117, v125
	ds_read_b64_tr_b16 v[124:125], v132 offset:36872
	v_pk_add_f32 v[78:79], v[118:119], v[78:79]
	v_mfma_f32_16x16x16_bf16 v[74:77], v[126:127], v[128:129], v[112:115]
	v_cvt_pk_bf16_f32 v127, v116, v117
	v_cvt_pk_bf16_f32 v126, v118, v119
	s_nop 0
	v_pk_add_f32 v[112:113], v[58:59], v[44:45]
	v_pk_add_f32 v[114:115], v[60:61], v[42:43]
	s_waitcnt lgkmcnt(2)
	v_mfma_f32_16x16x16_bf16 v[58:61], v[120:121], v[128:129], v[62:65]
	ds_read_b64_tr_b16 v[120:121], v132 offset:36864
	v_exp_f32_e32 v112, v112
	v_exp_f32_e32 v113, v113
	v_exp_f32_e32 v114, v114
	s_waitcnt lgkmcnt(2)
	v_mfma_f32_16x16x16_bf16 v[62:65], v[130:131], v[128:129], v[66:69]
	ds_read_b64_tr_b16 v[116:117], v132 offset:36928
	ds_read_b64_tr_b16 v[128:129], v132 offset:36936
	v_exp_f32_e32 v115, v115
	v_pk_add_f32 v[118:119], v[112:113], v[122:123]
	v_add_u32_e32 v122, v144, v105
	s_waitcnt lgkmcnt(2)
	v_mfma_f32_16x16x16_bf16 v[66:69], v[120:121], v[126:127], v[70:73]
	ds_read_b64_tr_b16 v[120:121], v122 offset:36872
	v_mfma_f32_16x16x16_bf16 v[70:73], v[124:125], v[126:127], v[74:77]
	s_nop 2
	v_add_f32_e64 v74, v114, v78
	v_add_f32_e64 v75, v115, v79
	v_pk_add_f32 v[76:77], v[54:55], v[44:45]
	v_pk_add_f32 v[78:79], v[56:57], v[42:43]
	s_waitcnt lgkmcnt(2)
	v_mfma_f32_16x16x16_bf16 v[54:57], v[116:117], v[126:127], v[58:61]
	ds_read_b64_tr_b16 v[116:117], v122 offset:36864
	v_cvt_pk_bf16_f32 v114, v114, v115
	v_cvt_pk_bf16_f32 v115, v112, v113
	ds_read_b64_tr_b16 v[112:113], v122 offset:36928
	ds_read_b64_tr_b16 v[122:123], v122 offset:36936
	s_waitcnt lgkmcnt(4)
; #define LAS __attribute__((address_space(3)))
; __device__ __forceinline__ void titem_finish(const TItem& t, int lane, const LAS unsigned char* buf) {
;     ...
;     const float wsc = t.scale;
; #pragma unroll
;     for (int j = 0; j < 4; ++j) { const int n = (lane >> 3) + 8 * j; const LAS float* s = sb + (8 * c) * 32 + 4 * ((n >> 2) ^ c) + (n & 3);
; #pragma unroll
;         for (int q = 0; q < 8; ++q) v[j][q] = s[32 * q] * wsc; }
;     if (t.f8) {
; #pragma unroll
;         for (int j = 0; j < 4; ++j) { const int n = (lane >> 3) + 8 * j;
;             int w0 = __builtin_amdgcn_cvt_pk_fp8_f32(v[j][0], v[j][1], 0, false); w0 = __builtin_amdgcn_cvt_pk_fp8_f32(v[j][2], v[j][3], w0, true);
;             int w1 = __builtin_amdgcn_cvt_pk_fp8_f32(v[j][4], v[j][5], 0, false); w1 = __builtin_amdgcn_cvt_pk_fp8_f32(v[j][6], v[j][7], w1, true);
;             u32x2 o; o.x = (unsigned)w0; o.y = (unsigned)w1;
;             __builtin_nontemporal_store(o, (u32x2*)((unsigned char*)t.WT + (size_t)(d0 + n) * t.K + k0 + 8 * c)); }
; __device__ __forceinline__ void phase_attn(Frame& F) {
;     ...
;         for (int T = 0; T < 9; ++T) {
;             u32x2 pw; pw.x = cvt_pk_bf16(St[T][0], St[T][1]); pw.y = cvt_pk_bf16(St[T][2], St[T][3]);
;             const s16x4 pb = __builtin_bit_cast(s16x4, pw);
;             LAS unsigned char* va = kb + ATT_VOFF + (16 * (w + T) + 4 * fq + (fr >> 2)) * ATT_ROWB + (8 * (fr & 3)) * 2;
; #pragma unroll
;             for (int dt = 0; dt < 4; ++dt) O[dt] = __builtin_amdgcn_mfma_f32_16x16x16bf16_1k(tr_read(va + 64 * (dt >> 1) + 8 * (dt & 1)), pb, O[dt], 0, 0, 0);
;         }
;         const float inv = 1.f / l;
;         bf16_t* op = (bf16_t*)((char*)part + (((size_t)cu.dsel * NTOK + (size_t)cu.b * SEQ + cu.r) * 512 + cu.h * 64) * 2 + (qrow * 1024u + 16u * fq));
; #pragma unroll
;         for (int u2 = 0; u2 < 2; ++u2) { u32x4 o4; o4.x = cvt_pk_bf16(O[2 * u2][0] * inv, O[2 * u2][1] * inv); o4.y = cvt_pk_bf16(O[2 * u2][2] * inv, O[2 * u2][3] * inv);
;             o4.z = cvt_pk_bf16(O[2 * u2 + 1][0] * inv, O[2 * u2 + 1][1] * inv); o4.w = cvt_pk_bf16(O[2 * u2 + 1][2] * inv, O[2 * u2 + 1][3] * inv); *(u32x4*)(op + 32 * u2) = o4; }
;         if (fq == 0) *(float*)((char*)lse + (((size_t)cu.dsel * NTOK + (size_t)cu.b * SEQ + cu.r) * 8 + cu.h) * 4 + qrow * 32u) = mx + __builtin_amdgcn_logf(l);
	v_mfma_f32_16x16x16_bf16 v[58:61], v[128:129], v[126:127], v[62:65]
	v_exp_f32_e32 v76, v76
	v_exp_f32_e32 v77, v77
	v_exp_f32_e32 v78, v78
	s_waitcnt lgkmcnt(2)
	v_mfma_f32_16x16x16_bf16 v[62:65], v[116:117], v[114:115], v[66:69]
	v_exp_f32_e32 v79, v79
	v_pk_add_f32 v[116:117], v[76:77], v[118:119]
	v_mfma_f32_16x16x16_bf16 v[66:69], v[120:121], v[114:115], v[70:73]
	s_nop 2
	v_add_f32_e64 v70, v42, v46
	v_add_f32_e64 v71, v43, v47
	s_waitcnt lgkmcnt(1)
	v_mfma_f32_16x16x16_bf16 v[42:45], v[112:113], v[114:115], v[54:57]
	v_exp_f32_e32 v72, v48
	v_exp_f32_e32 v73, v49
	v_exp_f32_e32 v70, v70
	v_add_u32_e32 v56, v144, v106
	ds_read_b64_tr_b16 v[54:55], v56 offset:36864
	s_waitcnt lgkmcnt(1)
	v_mfma_f32_16x16x16_bf16 v[46:49], v[122:123], v[114:115], v[58:61]
	v_exp_f32_e32 v71, v71
	v_cvt_pk_bf16_f32 v112, v78, v79
	v_cvt_pk_bf16_f32 v113, v76, v77
	ds_read_b64_tr_b16 v[58:59], v56 offset:36872
	ds_read_b64_tr_b16 v[76:77], v56 offset:36928
	ds_read_b64_tr_b16 v[114:115], v56 offset:36936
	s_waitcnt lgkmcnt(3)
	v_mfma_f32_16x16x16_bf16 v[54:57], v[54:55], v[112:113], v[62:65]
	s_nop 2
	v_add_f32_e64 v62, v78, v74
	v_add_f32_e64 v63, v79, v75
	v_pk_add_f32 v[64:65], v[72:73], v[116:117]
	v_pk_add_f32 v[62:63], v[70:71], v[62:63]
	v_add_u32_e32 v74, v144, v107
	s_waitcnt lgkmcnt(2)
	v_mfma_f32_16x16x16_bf16 v[58:61], v[58:59], v[112:113], v[66:69]
	s_nop 2
	v_pk_mov_b32 v[66:67], v[62:63], v[64:65] op_sel:[1,0]
	v_mov_b32_e32 v63, v65
	ds_read_b64_tr_b16 v[64:65], v74 offset:36864
	v_pk_add_f32 v[62:63], v[66:67], v[62:63]
	v_cvt_pk_bf16_f32 v66, v70, v71
	v_add_f32_e32 v75, v62, v63
	v_cvt_pk_bf16_f32 v67, v72, v73
	s_waitcnt lgkmcnt(2)
	v_mfma_f32_16x16x16_bf16 v[42:45], v[76:77], v[112:113], v[42:45]
	ds_read_b64_tr_b16 v[62:63], v74 offset:36872
	ds_read_b64_tr_b16 v[68:69], v74 offset:36928
	ds_read_b64_tr_b16 v[70:71], v74 offset:36936
	s_waitcnt lgkmcnt(3)
	v_mfma_f32_16x16x16_bf16 v[54:57], v[64:65], v[66:67], v[54:57]
	ds_bpermute_b32 v64, v142, v75
	s_waitcnt lgkmcnt(0)
	v_add_f32_e32 v72, v75, v64
	ds_bpermute_b32 v73, v143, v72
	v_mfma_f32_16x16x16_bf16 v[58:61], v[62:63], v[66:67], v[58:61]
	v_mfma_f32_16x16x16_bf16 v[62:65], v[68:69], v[66:67], v[42:45]
	s_waitcnt lgkmcnt(0)
	s_nop 1
	v_add_f32_e32 v43, v72, v73
	v_div_scale_f32 v68, s[64:65], v43, v43, 1.0
	v_mfma_f32_16x16x16_bf16 v[46:49], v[114:115], v[112:113], v[46:49]
	v_rcp_f32_e32 v69, v68
	v_lshlrev_b32_e32 v42, s35, v110
	s_ashr_i32 s35, s34, 31
	v_mfma_f32_16x16x16_bf16 v[44:47], v[70:71], v[66:67], v[46:49]
	s_lshl_b64 s[64:65], s[26:27], 16
	s_lshl_b64 s[34:35], s[34:35], 12
	s_ashr_i32 s26, s31, 31
	s_nop 0
	v_fma_f32 v48, -v68, v69, 1.0
	v_fmac_f32_e32 v69, v48, v69
	v_div_scale_f32 v48, vcc, 1.0, v43, 1.0
	v_mul_f32_e32 v49, v48, v69
	s_add_u32 s31, s34, s31
	v_fma_f32 v66, -v68, v49, v48
	s_addc_u32 s26, s35, s26
	v_fmac_f32_e32 v49, v66, v69
	s_add_u32 s34, s31, s64
	v_fma_f32 v48, -v68, v49, v48
	s_addc_u32 s35, s26, s65
	v_div_fmas_f32 v48, v48, v69, v49
	s_lshl_b32 s26, s30, 7
	s_lshl_b64 s[64:65], s[34:35], 10
	v_div_fixup_f32 v48, v48, v43, 1.0
	s_add_u32 s31, s24, s64
	v_lshl_or_b32 v49, v42, 10, v82
	s_addc_u32 s37, s25, s65
	v_pk_mul_f32 v[54:55], v[48:49], v[54:55] op_sel_hi:[0,1]
	v_pk_mul_f32 v[56:57], v[48:49], v[56:57] op_sel_hi:[0,1]
	s_add_u32 s64, s31, s26
	v_cvt_pk_bf16_f32 v54, v54, v55
	v_cvt_pk_bf16_f32 v55, v56, v57
	v_pk_mul_f32 v[56:57], v[48:49], v[58:59] op_sel_hi:[0,1]
	v_pk_mul_f32 v[58:59], v[48:49], v[60:61] op_sel_hi:[0,1]
	s_addc_u32 s65, s37, 0
	v_cvt_pk_bf16_f32 v56, v56, v57
	v_cvt_pk_bf16_f32 v57, v58, v59
	global_store_dwordx4 v49, v[54:57], s[64:65]
	v_pk_mul_f32 v[44:45], v[48:49], v[44:45] op_sel_hi:[0,1]
	s_nop 0
	v_pk_mul_f32 v[54:55], v[48:49], v[62:63] op_sel_hi:[0,1]
	v_pk_mul_f32 v[56:57], v[48:49], v[64:65] op_sel_hi:[0,1]
	v_cvt_pk_bf16_f32 v54, v54, v55
	v_cvt_pk_bf16_f32 v55, v56, v57
	v_cvt_pk_bf16_f32 v56, v44, v45
	v_pk_mul_f32 v[44:45], v[48:49], v[46:47] op_sel_hi:[0,1]
	v_cvt_pk_bf16_f32 v57, v44, v45
	global_store_dwordx4 v49, v[54:57], s[64:65] offset:64
	s_cmp_eq_u32 s95, 0
	s_cbranch_scc1 .Lcq_skip_l
	s_waitcnt vmcnt(12)
	v_pk_mul_f32 v[168:169], v[168:169], s[94:95] op_sel_hi:[1,0]
	v_pk_mul_f32 v[170:171], v[170:171], s[94:95] op_sel_hi:[1,0]
	v_pk_mul_f32 v[172:173], v[172:173], s[94:95] op_sel_hi:[1,0]
	v_pk_mul_f32 v[174:175], v[174:175], s[94:95] op_sel_hi:[1,0]
	v_pk_mul_f32 v[176:177], v[176:177], s[94:95] op_sel_hi:[1,0]
	v_pk_mul_f32 v[178:179], v[178:179], s[94:95] op_sel_hi:[1,0]
	v_pk_mul_f32 v[180:181], v[180:181], s[94:95] op_sel_hi:[1,0]
	v_pk_mul_f32 v[182:183], v[182:183], s[94:95] op_sel_hi:[1,0]
	s_cmp_eq_u32 s32, 3
	s_cbranch_scc0 .Lcq_q1_l
	v_cvt_pk_fp8_f32 v232, v168, v172
	v_cvt_pk_fp8_f32 v236, v169, v173
	v_cvt_pk_fp8_f32 v240, v170, v174
	v_cvt_pk_fp8_f32 v244, v171, v175
	v_cvt_pk_fp8_f32 v232, v176, v180 op_sel:[0,0,1]
	v_cvt_pk_fp8_f32 v236, v177, v181 op_sel:[0,0,1]
	v_cvt_pk_fp8_f32 v240, v178, v182 op_sel:[0,0,1]
	v_cvt_pk_fp8_f32 v244, v179, v183 op_sel:[0,0,1]
	s_branch .Lcq_skip_l
.Lcq_q1_l:
	s_cmp_eq_u32 s32, 2
	s_cbranch_scc0 .Lcq_q2_l
	v_cvt_pk_fp8_f32 v233, v168, v172
	v_cvt_pk_fp8_f32 v237, v169, v173
	v_cvt_pk_fp8_f32 v241, v170, v174
	v_cvt_pk_fp8_f32 v245, v171, v175
	v_cvt_pk_fp8_f32 v233, v176, v180 op_sel:[0,0,1]
	v_cvt_pk_fp8_f32 v237, v177, v181 op_sel:[0,0,1]
	v_cvt_pk_fp8_f32 v241, v178, v182 op_sel:[0,0,1]
	v_cvt_pk_fp8_f32 v245, v179, v183 op_sel:[0,0,1]
	s_branch .Lcq_skip_l
.Lcq_q2_l:
	s_cmp_eq_u32 s32, 1
	s_cbranch_scc0 .Lcq_q3_l
	v_cvt_pk_fp8_f32 v234, v168, v172
	v_cvt_pk_fp8_f32 v238, v169, v173
	v_cvt_pk_fp8_f32 v242, v170, v174
	v_cvt_pk_fp8_f32 v246, v171, v175
	v_cvt_pk_fp8_f32 v234, v176, v180 op_sel:[0,0,1]
	v_cvt_pk_fp8_f32 v238, v177, v181 op_sel:[0,0,1]
	v_cvt_pk_fp8_f32 v242, v178, v182 op_sel:[0,0,1]
	v_cvt_pk_fp8_f32 v246, v179, v183 op_sel:[0,0,1]
	s_branch .Lcq_skip_l
.Lcq_q3_l:
	v_cvt_pk_fp8_f32 v235, v168, v172
	v_cvt_pk_fp8_f32 v239, v169, v173
	v_cvt_pk_fp8_f32 v243, v170, v174
	v_cvt_pk_fp8_f32 v247, v171, v175
	v_cvt_pk_fp8_f32 v235, v176, v180 op_sel:[0,0,1]
	v_cvt_pk_fp8_f32 v239, v177, v181 op_sel:[0,0,1]
	v_cvt_pk_fp8_f32 v243, v178, v182 op_sel:[0,0,1]
	v_cvt_pk_fp8_f32 v247, v179, v183 op_sel:[0,0,1]
	s_lshr_b32 s99, s95, 2
	v_lshlrev_b32_e32 v250, 4, v248
	v_mad_u32_u24 v250, v249, s99, v250
	v_add_u32_e32 v251, s95, v250
	v_add_u32_e32 v254, s95, v251
	v_add_u32_e32 v255, s95, v254
	global_store_dwordx4 v250, v[232:235], s[92:93] nt
	global_store_dwordx4 v251, v[236:239], s[92:93] nt
	global_store_dwordx4 v254, v[240:243], s[92:93] nt
	global_store_dwordx4 v255, v[244:247], s[92:93] nt
	s_mov_b32 s100, 1

; __device__ __forceinline__ void convert_experts(Frame& F, int lo, int hi) {
;     ...
;         for (;;) {
;             const bool more = sq + 1 < ns; const int rn = more ? CONV_RIDX(sq + 1) : r;
;             if (more) { CONV_DESC(rn, tn); titem_issue(tn, F.lane, scr + (p ^ 1) * 8192); }
;             if (!more) asm volatile("s_waitcnt vmcnt(0)" ::: "memory");
;             else if (first) asm volatile("s_waitcnt vmcnt(8)" ::: "memory");
;             else asm volatile("s_waitcnt vmcnt(12)" ::: "memory");
;             titem_finish(tc, F.lane, scr + p * 8192);
;             asm volatile("s_waitcnt lgkmcnt(0)" ::: "memory");
;             if (!more) break;
;             tc = tn; r = rn; ++sq; p ^= 1; first = false;
;         }
.Lcq_tail:
	s_sub_u32 s32, s32, 1
	s_cmp_lt_i32 s32, 0
	s_cbranch_scc0 .Lcq_cont_t
	s_mov_b32 s32, 3
	s_mov_b32 s95, 0
	s_cmp_eq_u32 s90, 0
	s_cbranch_scc1 .Lcq_none_t
	s_sub_u32 s90, s90, 1
	s_lshr_b32 s98, s89, 6
	s_and_b32 s99, s89, 63
	s_mul_hi_u32 s100, s98, 0xaaaaaaab
	s_lshr_b32 s100, s100, 1
	s_mul_i32 s101, s100, 3
	s_sub_u32 s101, s98, s101
	s_cmp_lt_u32 s100, 256
	s_cselect_b32 s98, 0, 3
	s_cselect_b32 s95, s100, 0
	s_add_u32 s98, s98, s101
	s_lshl_b32 s98, s98, 1
	v_readlane_b32 s96, v253, s98
	s_add_u32 s98, s98, 1
	v_readlane_b32 s97, v253, s98
	s_lshl_b32 s95, s95, 20
	s_nop 3
	s_add_u32 s96, s96, s95
	s_addc_u32 s97, s97, 0
	s_cmp_eq_u32 s101, 2
	s_cbranch_scc1 .Lcq_down_t
	s_lshr_b32 s95, s99, 3
	s_and_b32 s99, s99, 7
	s_lshl_b32 s98, s95, 17
	s_add_u32 s96, s96, s98
	s_addc_u32 s97, s97, 0
	s_lshl_b32 s98, s99, 7
	s_add_u32 s96, s96, s98
	s_addc_u32 s97, s97, 0
	s_lshl_b32 s100, s100, 19
	s_lshr_b32 s98, s99, 2
	s_lshl_b32 s98, s98, 18
	s_add_u32 s100, s100, s98
	s_and_b32 s98, s99, 3
	s_lshl_b32 s98, s98, 15
	s_add_u32 s100, s100, s98
	s_lshl_b32 s98, s101, 17
	s_add_u32 s100, s100, s98
	s_lshl_b32 s98, s95, 7
	s_add_u32 s100, s100, s98
	v_readlane_b32 s92, v253, 12
	v_readlane_b32 s93, v253, 13
	s_mov_b32 s94, 0xc3317218
	s_cmp_eq_u32 s101, 0
	s_cselect_b32 s94, 0xc2b8aa3b, s94
	s_nop 3
	s_add_u32 s92, s92, s100
	s_addc_u32 s93, s93, 0
	s_movk_i32 s95, 0x400
	s_movk_i32 s98, 0x400
	s_branch .Lcq_go_t

; #define LAS __attribute__((address_space(3)))
; __device__ __forceinline__ void titem_finish(const TItem& t, int lane, const LAS unsigned char* buf) {
;     ...
;     const float wsc = t.scale;
; #pragma unroll
;     for (int j = 0; j < 4; ++j) { const int n = (lane >> 3) + 8 * j; const LAS float* s = sb + (8 * c) * 32 + 4 * ((n >> 2) ^ c) + (n & 3);
; #pragma unroll
;         for (int q = 0; q < 8; ++q) v[j][q] = s[32 * q] * wsc; }
;     if (t.f8) {
; #pragma unroll
;         for (int j = 0; j < 4; ++j) { const int n = (lane >> 3) + 8 * j;
;             int w0 = __builtin_amdgcn_cvt_pk_fp8_f32(v[j][0], v[j][1], 0, false); w0 = __builtin_amdgcn_cvt_pk_fp8_f32(v[j][2], v[j][3], w0, true);
;             int w1 = __builtin_amdgcn_cvt_pk_fp8_f32(v[j][4], v[j][5], 0, false); w1 = __builtin_amdgcn_cvt_pk_fp8_f32(v[j][6], v[j][7], w1, true);
;             u32x2 o; o.x = (unsigned)w0; o.y = (unsigned)w1;
;             __builtin_nontemporal_store(o, (u32x2*)((unsigned char*)t.WT + (size_t)(d0 + n) * t.K + k0 + 8 * c)); }
; __device__ __forceinline__ void convert_experts(Frame& F, int lo, int hi) {
;     ...
;         for (;;) {
;             const bool more = sq + 1 < ns; const int rn = more ? CONV_RIDX(sq + 1) : r;
;             if (more) { CONV_DESC(rn, tn); titem_issue(tn, F.lane, scr + (p ^ 1) * 8192); }
;             if (!more) asm volatile("s_waitcnt vmcnt(0)" ::: "memory");
;             else if (first) asm volatile("s_waitcnt vmcnt(8)" ::: "memory");
;             else asm volatile("s_waitcnt vmcnt(12)" ::: "memory");
;             titem_finish(tc, F.lane, scr + p * 8192);
;             asm volatile("s_waitcnt lgkmcnt(0)" ::: "memory");
;             if (!more) break;
.Lcq_none_t:
	s_cmp_eq_u32 s95, 0
	s_cbranch_scc1 .Lcq_tail_done
	s_waitcnt vmcnt(0)
	s_cmp_eq_u32 s95, 0
	s_cbranch_scc1 .Lcq_skip_t
	s_waitcnt vmcnt(0)
	v_pk_mul_f32 v[168:169], v[168:169], s[94:95] op_sel_hi:[1,0]
	v_pk_mul_f32 v[170:171], v[170:171], s[94:95] op_sel_hi:[1,0]
	v_pk_mul_f32 v[172:173], v[172:173], s[94:95] op_sel_hi:[1,0]
	v_pk_mul_f32 v[174:175], v[174:175], s[94:95] op_sel_hi:[1,0]
	v_pk_mul_f32 v[176:177], v[176:177], s[94:95] op_sel_hi:[1,0]
	v_pk_mul_f32 v[178:179], v[178:179], s[94:95] op_sel_hi:[1,0]
	v_pk_mul_f32 v[180:181], v[180:181], s[94:95] op_sel_hi:[1,0]
	v_pk_mul_f32 v[182:183], v[182:183], s[94:95] op_sel_hi:[1,0]
	s_cmp_eq_u32 s32, 3
	s_cbranch_scc0 .Lcq_q1_t
	v_cvt_pk_fp8_f32 v232, v168, v172
	v_cvt_pk_fp8_f32 v236, v169, v173
	v_cvt_pk_fp8_f32 v240, v170, v174
	v_cvt_pk_fp8_f32 v244, v171, v175
	v_cvt_pk_fp8_f32 v232, v176, v180 op_sel:[0,0,1]
	v_cvt_pk_fp8_f32 v236, v177, v181 op_sel:[0,0,1]
	v_cvt_pk_fp8_f32 v240, v178, v182 op_sel:[0,0,1]
	v_cvt_pk_fp8_f32 v244, v179, v183 op_sel:[0,0,1]
	s_branch .Lcq_skip_t
